# attention epilogue: 8 LDS reads in flight then 8 stores (saddr form)
# speedup vs baseline: 1.0806x; 1.0007x over previous
.LBB2_42:
	v_mov_b32_e32 v33, v32
	s_nop 1
	v_permlane32_swap_b32_e32 v32, v33
	v_add_f32_e32 v32, v32, v33
	v_div_scale_f32 v33, s[0:1], v32, v32, 1.0
	v_rcp_f32_e32 v34, v33
	s_mulk_i32 s19, 0x2200
	s_waitcnt vmcnt(0)
	s_waitcnt lgkmcnt(0)
	v_fma_f32 v35, -v33, v34, 1.0
	v_fmac_f32_e32 v34, v35, v34
	v_div_scale_f32 v35, vcc, 1.0, v32, 1.0
	v_mul_f32_e32 v36, v35, v34
	v_fma_f32 v37, -v33, v36, v35
	v_fmac_f32_e32 v36, v37, v34
	v_fma_f32 v33, -v33, v36, v35
	v_div_fmas_f32 v33, v33, v34, v36
	v_div_fixup_f32 v32, v33, v32, 1.0
	v_mul_u32_u24_e32 v33, 0x110, v162
	v_add3_u32 v33, s19, v33, v148
	v_pk_mul_f32 v[16:17], v[32:33], v[16:17] op_sel_hi:[0,1]
	v_pk_mul_f32 v[0:1], v[32:33], v[0:1] op_sel_hi:[0,1]
	v_pk_mul_f32 v[18:19], v[32:33], v[18:19] op_sel_hi:[0,1]
	v_pk_mul_f32 v[2:3], v[32:33], v[2:3] op_sel_hi:[0,1]
	s_barrier
	ds_write_b128 v33, v[16:19]
	ds_write_b128 v33, v[0:3] offset:128
	v_pk_mul_f32 v[0:1], v[32:33], v[20:21] op_sel_hi:[0,1]
	v_pk_mul_f32 v[4:5], v[32:33], v[4:5] op_sel_hi:[0,1]
	v_pk_mul_f32 v[2:3], v[32:33], v[22:23] op_sel_hi:[0,1]
	s_add_u32 s0, s12, s18
	v_pk_mul_f32 v[6:7], v[32:33], v[6:7] op_sel_hi:[0,1]
	ds_write_b128 v33, v[0:3] offset:32
	ds_write_b128 v33, v[4:7] offset:160
	v_pk_mul_f32 v[0:1], v[32:33], v[24:25] op_sel_hi:[0,1]
	v_pk_mul_f32 v[4:5], v[32:33], v[8:9] op_sel_hi:[0,1]
	v_pk_mul_f32 v[2:3], v[32:33], v[26:27] op_sel_hi:[0,1]
	s_addc_u32 s1, s13, 0
	v_pk_mul_f32 v[6:7], v[32:33], v[10:11] op_sel_hi:[0,1]
	ds_write_b128 v33, v[0:3] offset:64
	ds_write_b128 v33, v[4:7] offset:192
	v_pk_mul_f32 v[0:1], v[32:33], v[28:29] op_sel_hi:[0,1]
	v_pk_mul_f32 v[4:5], v[32:33], v[12:13] op_sel_hi:[0,1]
	v_pk_mul_f32 v[2:3], v[32:33], v[30:31] op_sel_hi:[0,1]
	s_lshl_b64 s[0:1], s[0:1], 8
	v_pk_mul_f32 v[6:7], v[32:33], v[14:15] op_sel_hi:[0,1]
	ds_write_b128 v33, v[0:3] offset:96
	ds_write_b128 v33, v[4:7] offset:224
	s_add_u32 s0, s8, s0
	v_lshrrev_b32_e32 v0, 4, v163
	v_mov_b32_e32 v5, 0
	s_addc_u32 s1, s9, s1
	v_lshlrev_b32_e32 v4, 2, v149
	v_lshlrev_b32_e32 v6, 8, v0
	v_mov_b32_e32 v7, v5
	v_lshlrev_b32_e32 v1, 4, v149
	v_mul_u32_u24_e32 v0, 0x110, v0
	v_lshl_add_u32 v8, v4, 2, v6
	v_add_u32_e32 v9, 0x1000, v8
	v_add3_u32 v12, s19, v1, v0
	ds_read_b128 v[16:19], v12
	ds_read_b128 v[20:23], v12 offset:1088
	ds_read_b128 v[24:27], v12 offset:2176
	ds_read_b128 v[28:31], v12 offset:3264
	ds_read_b128 v[32:35], v12 offset:4352
	ds_read_b128 v[36:39], v12 offset:5440
	ds_read_b128 v[40:43], v12 offset:6528
	ds_read_b128 v[44:47], v12 offset:7616
	s_waitcnt lgkmcnt(7)
	global_store_dwordx4 v8, v[16:19], s[0:1] sc1
	s_waitcnt lgkmcnt(6)
	global_store_dwordx4 v8, v[20:23], s[0:1] offset:1024 sc1
	s_waitcnt lgkmcnt(5)
	global_store_dwordx4 v8, v[24:27], s[0:1] offset:2048 sc1
	s_waitcnt lgkmcnt(4)
	global_store_dwordx4 v8, v[28:31], s[0:1] offset:3072 sc1
	s_waitcnt lgkmcnt(3)
	global_store_dwordx4 v9, v[32:35], s[0:1] sc1
	s_waitcnt lgkmcnt(2)
	global_store_dwordx4 v9, v[36:39], s[0:1] offset:1024 sc1
	s_waitcnt lgkmcnt(1)
	global_store_dwordx4 v9, v[40:43], s[0:1] offset:2048 sc1
	s_waitcnt lgkmcnt(0)
	global_store_dwordx4 v9, v[44:47], s[0:1] offset:3072 sc1
	s_endpgm
